# v87: M3 retention loop: the end-of-item barrier moved below the next item's address math and load requests (it only has to precede the LDS writes)
# speedup vs baseline: 1.0007x; 1.0007x over previous
.LBB0_550:
	s_add_i32 s3, s3, s65
	s_cmp_ge_i32 s3, s81
	s_cbranch_scc1 .LBB0_561

.LBB0_555:
	s_and_b32 s33, s3, 1
	s_lshl_b32 s4, s33, 1
	s_add_i32 s14, s4, s18
	s_mul_i32 s4, s10, 0x1100
	s_lshl_b32 s5, s11, 7
	s_add_i32 s45, s4, s5
	s_lshl_b32 s22, s14, 6
	v_or_b32_e32 v2, s45, v116
	v_mov_b64_e32 v[50:51], s[88:89]
	s_mul_i32 s5, s14, 0x44
	s_ashr_i32 s23, s22, 31
	v_mad_i64_i32 v[2:3], s[14:15], v2, s60, v[50:51]
	s_lshl_b64 s[14:15], s[22:23], 1
	v_mov_b32_e32 v101, v0
	v_lshl_add_u64 v[2:3], v[2:3], 0, s[14:15]
	v_or_b32_e32 v10, s45, v117
	v_lshl_add_u64 v[2:3], v[2:3], 0, v[100:101]
	v_mad_i64_i32 v[10:11], s[26:27], v10, s60, v[50:51]
	s_mul_i32 s4, s10, 0x110
	v_add_co_u32_e32 v6, vcc, s78, v2
	v_lshl_add_u64 v[10:11], v[10:11], 0, s[14:15]
	v_or_b32_e32 v18, s45, v118
	s_add_i32 s4, s4, s5
	v_addc_co_u32_e32 v7, vcc, 0, v3, vcc
	v_lshl_add_u64 v[10:11], v[10:11], 0, v[100:101]
	v_mad_i64_i32 v[18:19], s[26:27], v18, s60, v[50:51]
	s_add_i32 s4, s4, s11
	v_add_co_u32_e32 v14, vcc, s78, v10
	v_lshl_add_u64 v[18:19], v[18:19], 0, s[14:15]
	v_or_b32_e32 v26, s45, v119
	s_ashr_i32 s5, s4, 31
	v_addc_co_u32_e32 v15, vcc, 0, v11, vcc
	v_lshl_add_u64 v[18:19], v[18:19], 0, v[100:101]
	v_mad_i64_i32 v[26:27], s[26:27], v26, s60, v[50:51]
	s_lshl_b64 s[10:11], s[4:5], 13
	s_add_i32 s4, s4, 34
	v_add_co_u32_e32 v22, vcc, s78, v18
	v_lshl_add_u64 v[26:27], v[26:27], 0, s[14:15]
	s_ashr_i32 s5, s4, 31
	v_addc_co_u32_e32 v23, vcc, 0, v19, vcc
	v_lshl_add_u64 v[26:27], v[26:27], 0, v[100:101]
	s_lshl_b64 s[4:5], s[4:5], 13
	v_add_co_u32_e32 v30, vcc, s78, v26
	s_cmp_eq_u32 s33, 0
	s_nop 0
	v_addc_co_u32_e32 v31, vcc, 0, v27, vcc
	s_cselect_b64 vcc, -1, 0
	s_add_u32 s10, s66, s10
	s_addc_u32 s11, s67, s11
	s_add_u32 s4, s66, s4
	s_addc_u32 s5, s67, s5
	v_or_b32_e32 v104, s45, v109
	global_load_dwordx4 v[2:5], v[6:7], off offset:512
	s_nop 0
	global_load_dwordx4 v[6:9], v[6:7], off
	s_nop 0
	global_load_dwordx4 v[10:13], v[14:15], off offset:512
	s_nop 0
	global_load_dwordx4 v[14:17], v[14:15], off
	s_nop 0
	global_load_dwordx4 v[18:21], v[22:23], off offset:512
	s_nop 0
	global_load_dwordx4 v[22:25], v[22:23], off
	s_nop 0
	global_load_dwordx4 v[26:29], v[30:31], off offset:512
	s_nop 0
	global_load_dwordx4 v[30:33], v[30:31], off
	s_nop 0
	global_load_dwordx4 v[34:37], v125, s[10:11]
	global_load_dwordx4 v[38:41], v125, s[4:5]
	global_load_dwordx4 v[42:45], v126, s[10:11]
	global_load_dwordx4 v[46:49], v126, s[4:5]
	v_mad_i64_i32 v[106:107], s[4:5], v104, s60, v[50:51]
	v_lshl_add_u64 v[50:51], v[106:107], 0, s[14:15]
	v_mov_b32_e32 v103, v0
	v_lshl_add_u64 v[50:51], v[50:51], 0, v[102:103]
	global_load_dwordx4 v[78:81], v[50:51], off offset:3584
	global_load_dwordx4 v[74:77], v[50:51], off offset:3616
	global_load_dwordx4 v[70:73], v[50:51], off offset:3648
	global_load_dwordx4 v[66:69], v[50:51], off offset:3680
	v_cndmask_b32_e32 v50, v142, v1, vcc
	s_mov_b32 s10, 0
	v_mul_f32_e32 v101, 0xbfb8aa3b, v50
	v_ashrrev_i32_e32 v105, 31, v104
	s_mov_b64 s[4:5], -1
	v_cndmask_b32_e32 v152, v143, v141, vcc
	v_mul_f32_e32 v103, 0xbfb8aa3b, v152
	v_mul_f32_e32 v167, 0xbf800000, v101
	v_mul_f32_e32 v168, 0xc0000000, v101
	v_mul_f32_e32 v169, 0xc0400000, v101
	v_mul_f32_e32 v170, 0xc1000000, v101
	v_mul_f32_e32 v171, 0x3f800000, v103
	v_mul_f32_e32 v172, 0x40000000, v103
	v_mul_f32_e32 v173, 0x40400000, v103
	v_mul_f32_e32 v174, 0x41000000, v103
	v_exp_f32_e32 v167, v167
	v_exp_f32_e32 v168, v168
	v_exp_f32_e32 v169, v169
	v_exp_f32_e32 v170, v170
	v_exp_f32_e32 v171, v171
	v_exp_f32_e32 v172, v172
	v_exp_f32_e32 v173, v173
	v_exp_f32_e32 v174, v174
	v_lshl_add_u64 v[152:153], s[22:23], 1, v[106:107]
	v_lshlrev_b32_e32 v154, 1, v82
	v_mov_b32_e32 v155, v0
	v_lshl_add_u64 v[152:153], v[152:153], 0, v[154:155]
	s_mov_b64 s[98:99], 0x1400
	ds_read_b64 v[156:157], v0 offset:640
	v_lshl_add_u64 v[154:155], v[152:153], 0, s[98:99]
	v_add_co_u32_e32 v152, vcc, s78, v152
	s_lshl_b64 s[98:99], s[24:25], 2
	s_lshl_b64 s[100:101], s[22:23], 2
	v_addc_co_u32_e32 v153, vcc, 0, v153, vcc
	global_load_dwordx2 v[222:223], v[152:153], off offset:1024
	global_load_dwordx2 v[224:225], v[154:155], off offset:16
	global_load_dwordx2 v[226:227], v[154:155], off offset:32
	global_load_dwordx2 v[228:229], v[154:155], off offset:48
	global_load_dwordx2 v[230:231], v[154:155], off offset:64
	global_load_dwordx2 v[232:233], v[154:155], off offset:80
	global_load_dwordx2 v[234:235], v[154:155], off offset:96
	global_load_dwordx2 v[236:237], v[154:155], off offset:112
	s_add_u32 s98, s98, s100
	s_addc_u32 s99, s99, s101
	s_waitcnt lgkmcnt(0)
	v_readfirstlane_b32 s100, v156
	v_readfirstlane_b32 s101, v157
	v_lshlrev_b32_e32 v152, 2, v82
	s_add_u32 s98, s100, s98
	s_addc_u32 s99, s101, s99
	global_load_dwordx4 v[238:241], v152, s[98:99]
	global_load_dwordx4 v[242:245], v152, s[98:99] offset:32
	global_load_dwordx4 v[246:249], v152, s[98:99] offset:64
	global_load_dwordx4 v[250:253], v152, s[98:99] offset:96
	global_load_dwordx4 v[200:203], v152, s[98:99] offset:128
	global_load_dwordx4 v[204:207], v152, s[98:99] offset:160
	global_load_dwordx4 v[214:217], v152, s[98:99] offset:192
	global_load_dwordx4 v[192:195], v152, s[98:99] offset:224
	s_barrier
	s_waitcnt vmcnt(31)
	ds_write_b128 v127, v[2:5]
	s_waitcnt vmcnt(30)
	ds_write_b128 v128, v[6:9] offset:16384
	s_waitcnt vmcnt(29)
	ds_write_b128 v129, v[10:13]
	s_waitcnt vmcnt(28)
	ds_write_b128 v130, v[14:17] offset:16384
	s_waitcnt vmcnt(27)
	ds_write_b128 v127, v[18:21] offset:8192
	s_waitcnt vmcnt(26)
	ds_write_b128 v131, v[22:25] offset:16384
	s_waitcnt vmcnt(25)
	ds_write_b128 v132, v[26:29] offset:8192
	s_waitcnt vmcnt(24)
	ds_write_b128 v133, v[30:33] offset:16384
	s_waitcnt vmcnt(23)
	ds_write_b128 v128, v[34:37] offset:32768
	s_waitcnt vmcnt(22)
	ds_write_b128 v128, v[38:41] offset:40960
	s_waitcnt vmcnt(21)
	ds_write_b128 v130, v[42:45] offset:32768
	s_waitcnt vmcnt(20)
	ds_write_b128 v130, v[46:49] offset:40960
	v_mov_b32_e32 v18, 0
	v_mov_b32_e32 v19, v18
	v_mov_b32_e32 v20, v18
	v_mov_b32_e32 v21, v18
	v_mov_b32_e32 v22, v18
	v_mov_b32_e32 v23, v18
	v_mov_b32_e32 v24, v18
	v_mov_b32_e32 v25, v18
	v_mov_b32_e32 v26, v18
	v_mov_b32_e32 v27, v18
	v_mov_b32_e32 v28, v18
	v_mov_b32_e32 v29, v18
	v_mov_b32_e32 v30, v18
	v_mov_b32_e32 v31, v18
	v_mov_b32_e32 v32, v18
	v_mov_b32_e32 v33, v18
	v_mov_b32_e32 v2, v18
	v_mov_b32_e32 v3, v18
	v_mov_b32_e32 v4, v18
	v_mov_b32_e32 v5, v18
	v_mov_b32_e32 v6, v18
	v_mov_b32_e32 v7, v18
	v_mov_b32_e32 v8, v18
	v_mov_b32_e32 v9, v18
	v_mov_b32_e32 v10, v18
	v_mov_b32_e32 v11, v18
	v_mov_b32_e32 v12, v18
	v_mov_b32_e32 v13, v18
	v_mov_b32_e32 v14, v18
	v_mov_b32_e32 v15, v18
	v_mov_b32_e32 v16, v18
	v_mov_b32_e32 v17, v18
	s_waitcnt lgkmcnt(0)
	s_barrier
